# baseline (speedup 1.0000x reference)
.LBB2_21:
	v_cvt_pk_f16_f32 v13, v13, v13
	v_cvt_pk_f16_f32 v12, v12, v12
	v_cvt_pk_f16_f32 v11, v11, v11
	v_cvt_pk_f16_f32 v10, v10, v10
	ds_write_b128 v98, v[10:13]
	ds_write_b32 v98, v17 offset:16
	s_and_saveexec_b64 s[6:7], s[4:5]
	ds_write_b32 v99, v86 offset:16
	s_or_b64 exec, exec, s[6:7]
	s_sub_i32 s6, s23, s24
	s_cmp_lt_i32 s6, 1
	s_cbranch_scc1 .LBB2_26
	ds_read2_b32 v[10:11], v96 offset0:20 offset1:28
	ds_read2_b32 v[12:13], v96 offset0:4 offset1:12
	s_min_i32 s6, s6, 16
	s_mov_b32 s7, 0
	v_mov_b32_e32 v118, v96
	s_waitcnt lgkmcnt(1)
	v_lshl_or_b32 v58, v11, 8, v72
	s_waitcnt lgkmcnt(0)
	v_lshl_or_b32 v12, v12, 8, v72
	v_lshl_or_b32 v13, v13, 8, v72
	v_lshl_or_b32 v54, v10, 8, v72
	global_load_dwordx4 v[14:17], v12, s[16:17]
	s_nop 0
	global_load_dwordx4 v[10:13], v13, s[16:17]
	s_nop 0
	global_load_dwordx4 v[54:57], v54, s[16:17]
	s_nop 0
	global_load_dwordx4 v[58:61], v58, s[16:17]
	.p2align 3
.LBB2_25:
	s_sub_i32 s60, s6, s7
	s_cmp_lt_i32 s60, 4
	s_cbranch_scc1 .Lmy_part
	ds_read_b128 v[120:123], v118
	ds_read_b128 v[124:127], v118 offset:32
	ds_read2_b32 v[6:7], v118 offset0:36 offset1:44
	s_waitcnt vmcnt(3) lgkmcnt(2)
	v_pk_fma_f16 v109, v14, v120, v109
	v_pk_fma_f16 v97, v14, v121, v97
	v_pk_fma_f16 v90, v14, v122, v90
	v_pk_fma_f16 v85, v14, v123, v85
	v_pk_fma_f16 v108, v15, v120, v108
	v_pk_fma_f16 v95, v15, v121, v95
	v_pk_fma_f16 v89, v15, v122, v89
	v_pk_fma_f16 v84, v15, v123, v84
	v_pk_fma_f16 v107, v16, v120, v107
	v_pk_fma_f16 v94, v16, v121, v94
	v_pk_fma_f16 v88, v16, v122, v88
	v_pk_fma_f16 v82, v16, v123, v82
	v_pk_fma_f16 v105, v17, v120, v105
	v_pk_fma_f16 v92, v17, v121, v92
	v_pk_fma_f16 v87, v17, v122, v87
	v_pk_fma_f16 v81, v17, v123, v81
	s_waitcnt lgkmcnt(0)
	v_lshl_or_b32 v14, v6, 8, v72
	global_load_dwordx4 v[14:17], v14, s[16:17]
	ds_read_b128 v[120:123], v118 offset:64
	s_waitcnt vmcnt(3)
	v_pk_fma_f16 v109, v10, v124, v109
	v_pk_fma_f16 v97, v10, v125, v97
	v_pk_fma_f16 v90, v10, v126, v90
	v_pk_fma_f16 v85, v10, v127, v85
	v_pk_fma_f16 v108, v11, v124, v108
	v_pk_fma_f16 v95, v11, v125, v95
	v_pk_fma_f16 v89, v11, v126, v89
	v_pk_fma_f16 v84, v11, v127, v84
	v_pk_fma_f16 v107, v12, v124, v107
	v_pk_fma_f16 v94, v12, v125, v94
	v_pk_fma_f16 v88, v12, v126, v88
	v_pk_fma_f16 v82, v12, v127, v82
	v_pk_fma_f16 v105, v13, v124, v105
	v_pk_fma_f16 v92, v13, v125, v92
	v_pk_fma_f16 v87, v13, v126, v87
	v_pk_fma_f16 v81, v13, v127, v81
	v_lshl_or_b32 v10, v7, 8, v72
	global_load_dwordx4 v[10:13], v10, s[16:17]
	ds_read2_b32 v[8:9], v118 offset0:52 offset1:60
	ds_read_b128 v[124:127], v118 offset:96
	s_add_i32 s7, s7, 4
	s_waitcnt vmcnt(3) lgkmcnt(2)
	v_pk_fma_f16 v109, v54, v120, v109
	v_pk_fma_f16 v97, v54, v121, v97
	v_pk_fma_f16 v90, v54, v122, v90
	v_pk_fma_f16 v85, v54, v123, v85
	v_pk_fma_f16 v108, v55, v120, v108
	v_pk_fma_f16 v95, v55, v121, v95
	v_pk_fma_f16 v89, v55, v122, v89
	v_pk_fma_f16 v84, v55, v123, v84
	v_pk_fma_f16 v107, v56, v120, v107
	v_pk_fma_f16 v94, v56, v121, v94
	v_pk_fma_f16 v88, v56, v122, v88
	v_pk_fma_f16 v82, v56, v123, v82
	v_pk_fma_f16 v105, v57, v120, v105
	v_pk_fma_f16 v92, v57, v121, v92
	v_pk_fma_f16 v87, v57, v122, v87
	v_pk_fma_f16 v81, v57, v123, v81
	s_waitcnt lgkmcnt(1)
	v_lshl_or_b32 v54, v8, 8, v72
	global_load_dwordx4 v[54:57], v54, s[16:17]
	v_add_u32_e32 v118, 0x80, v118
	s_waitcnt vmcnt(3) lgkmcnt(0)
	v_pk_fma_f16 v109, v58, v124, v109
	v_pk_fma_f16 v97, v58, v125, v97
	v_pk_fma_f16 v90, v58, v126, v90
	v_pk_fma_f16 v85, v58, v127, v85
	v_pk_fma_f16 v108, v59, v124, v108
	v_pk_fma_f16 v95, v59, v125, v95
	v_pk_fma_f16 v89, v59, v126, v89
	v_pk_fma_f16 v84, v59, v127, v84
	v_pk_fma_f16 v107, v60, v124, v107
	v_pk_fma_f16 v94, v60, v125, v94
	v_pk_fma_f16 v88, v60, v126, v88
	v_pk_fma_f16 v82, v60, v127, v82
	v_pk_fma_f16 v105, v61, v124, v105
	v_pk_fma_f16 v92, v61, v125, v92
	v_pk_fma_f16 v87, v61, v126, v87
	v_pk_fma_f16 v81, v61, v127, v81
	v_lshl_or_b32 v58, v9, 8, v72
	global_load_dwordx4 v[58:61], v58, s[16:17]
	s_cmp_ge_i32 s7, s6
	s_cbranch_scc0 .LBB2_25
	s_branch .LBB2_26
	.p2align 3
.Lmy_part:
	s_waitcnt vmcnt(3)
	ds_read_b128 v[120:123], v118
	s_waitcnt lgkmcnt(0)
	v_pk_fma_f16 v109, v14, v120, v109
	v_pk_fma_f16 v97, v14, v121, v97
	v_pk_fma_f16 v90, v14, v122, v90
	v_pk_fma_f16 v85, v14, v123, v85
	v_pk_fma_f16 v108, v15, v120, v108
	v_pk_fma_f16 v95, v15, v121, v95
	v_pk_fma_f16 v89, v15, v122, v89
	v_pk_fma_f16 v84, v15, v123, v84
	v_pk_fma_f16 v107, v16, v120, v107
	v_pk_fma_f16 v94, v16, v121, v94
	v_pk_fma_f16 v88, v16, v122, v88
	v_pk_fma_f16 v82, v16, v123, v82
	v_pk_fma_f16 v105, v17, v120, v105
	v_pk_fma_f16 v92, v17, v121, v92
	v_pk_fma_f16 v87, v17, v122, v87
	v_pk_fma_f16 v81, v17, v123, v81
	s_cmp_lt_i32 s60, 2
	s_cbranch_scc1 .LBB2_26
	s_waitcnt vmcnt(2)
	ds_read_b128 v[124:127], v118 offset:32
	s_waitcnt lgkmcnt(0)
	v_pk_fma_f16 v109, v10, v124, v109
	v_pk_fma_f16 v97, v10, v125, v97
	v_pk_fma_f16 v90, v10, v126, v90
	v_pk_fma_f16 v85, v10, v127, v85
	v_pk_fma_f16 v108, v11, v124, v108
	v_pk_fma_f16 v95, v11, v125, v95
	v_pk_fma_f16 v89, v11, v126, v89
	v_pk_fma_f16 v84, v11, v127, v84
	v_pk_fma_f16 v107, v12, v124, v107
	v_pk_fma_f16 v94, v12, v125, v94
	v_pk_fma_f16 v88, v12, v126, v88
	v_pk_fma_f16 v82, v12, v127, v82
	v_pk_fma_f16 v105, v13, v124, v105
	v_pk_fma_f16 v92, v13, v125, v92
	v_pk_fma_f16 v87, v13, v126, v87
	v_pk_fma_f16 v81, v13, v127, v81
	s_cmp_lt_i32 s60, 3
	s_cbranch_scc1 .LBB2_26
	s_waitcnt vmcnt(1)
	ds_read_b128 v[120:123], v118 offset:64
	s_waitcnt lgkmcnt(0)
	v_pk_fma_f16 v109, v54, v120, v109
	v_pk_fma_f16 v97, v54, v121, v97
	v_pk_fma_f16 v90, v54, v122, v90
	v_pk_fma_f16 v85, v54, v123, v85
	v_pk_fma_f16 v108, v55, v120, v108
	v_pk_fma_f16 v95, v55, v121, v95
	v_pk_fma_f16 v89, v55, v122, v89
	v_pk_fma_f16 v84, v55, v123, v84
	v_pk_fma_f16 v107, v56, v120, v107
	v_pk_fma_f16 v94, v56, v121, v94
	v_pk_fma_f16 v88, v56, v122, v88
	v_pk_fma_f16 v82, v56, v123, v82
	v_pk_fma_f16 v105, v57, v120, v105
	v_pk_fma_f16 v92, v57, v121, v92
	v_pk_fma_f16 v87, v57, v122, v87
	v_pk_fma_f16 v81, v57, v123, v81
